# grid barrier poll reads 2x16 B (the 8 per-XCD flags) instead of 4x16 B per iteration
# speedup vs baseline: 1.0177x; 1.0024x over previous
; __device__ __forceinline__ unsigned xb_ld(unsigned* p)              { return __hip_atomic_load(p, __ATOMIC_RELAXED, __HIP_MEMORY_SCOPE_AGENT); }
; __device__ __forceinline__ void xcd_barrier_complete(unsigned* bar, unsigned x, unsigned& nloc, unsigned& nx) {
;     const unsigned G = gridDim.x * gridDim.y * gridDim.z;
;     unsigned sum, cnt, mine, sp = 0u;
;     for (;;) {
;         sum = 0u; cnt = 0u; mine = 0u;
; #pragma unroll
;         for (unsigned j = 0; j < 16; ++j) { const unsigned c = xb_ld(&bar[XB_XCNT(j)]); sum += c; cnt += (c > 0u) ? 1u : 0u; mine = (j == x) ? c : mine; }
;         if (sum == G) break;
;         __builtin_amdgcn_s_sleep(1);
;         if ((++sp & 255u) == 0u) { if (xb_ld(&bar[XB_TMO])) break; if (sp > XB_SPIN_CAP) { atomicAdd(&bar[XB_TMO], 1u); break; } }
;     }
;     nloc = mine > 0u ? mine : 1u; nx = cnt > 0u ? cnt : 1u;
; }
.Lxbar0_spin:
	global_load_dwordx4 v[4:7], v20, s[6:7] sc1
	global_load_dwordx4 v[8:11], v20, s[6:7] offset:16 sc1
	s_waitcnt vmcnt(0)
	v_add3_u32 v2, v4, v5, v6
	v_add3_u32 v2, v2, v7, v8
	v_add3_u32 v2, v2, v9, v10
	v_add_u32_e32 v2, v2, v11
	v_cmp_ge_u32_e32 vcc, v2, v1
	s_cbranch_vccnz .Lxbar0_done
	s_sleep 1
	s_add_i32 s2, s2, 1
	s_cmp_lt_u32 s2, 0x80000
	s_cbranch_scc1 .Lxbar0_spin

; __device__ __forceinline__ unsigned xb_ld(unsigned* p)              { return __hip_atomic_load(p, __ATOMIC_RELAXED, __HIP_MEMORY_SCOPE_AGENT); }
; __device__ __forceinline__ void xcd_barrier_complete(unsigned* bar, unsigned x, unsigned& nloc, unsigned& nx) {
;     const unsigned G = gridDim.x * gridDim.y * gridDim.z;
;     unsigned sum, cnt, mine, sp = 0u;
;     for (;;) {
;         sum = 0u; cnt = 0u; mine = 0u;
; #pragma unroll
;         for (unsigned j = 0; j < 16; ++j) { const unsigned c = xb_ld(&bar[XB_XCNT(j)]); sum += c; cnt += (c > 0u) ? 1u : 0u; mine = (j == x) ? c : mine; }
;         if (sum == G) break;
;         __builtin_amdgcn_s_sleep(1);
;         if ((++sp & 255u) == 0u) { if (xb_ld(&bar[XB_TMO])) break; if (sp > XB_SPIN_CAP) { atomicAdd(&bar[XB_TMO], 1u); break; } }
;     }
;     nloc = mine > 0u ? mine : 1u; nx = cnt > 0u ? cnt : 1u;
; }
.Lxbar1_spin:
	global_load_dwordx4 v[4:7], v20, s[8:9] sc1
	global_load_dwordx4 v[8:11], v20, s[8:9] offset:16 sc1
	s_waitcnt vmcnt(0)
	v_add3_u32 v1, v4, v5, v6
	v_add3_u32 v1, v1, v7, v8
	v_add3_u32 v1, v1, v9, v10
	v_add_u32_e32 v1, v1, v11
	v_cmp_ge_u32_e32 vcc, v1, v3
	s_cbranch_vccnz .Lxbar1_done
	s_sleep 1
	s_add_i32 s4, s4, 1
	s_cmp_lt_u32 s4, 0x80000
	s_cbranch_scc1 .Lxbar1_spin

; __device__ __forceinline__ unsigned xb_ld(unsigned* p)              { return __hip_atomic_load(p, __ATOMIC_RELAXED, __HIP_MEMORY_SCOPE_AGENT); }
; __device__ __forceinline__ void xcd_barrier_complete(unsigned* bar, unsigned x, unsigned& nloc, unsigned& nx) {
;     const unsigned G = gridDim.x * gridDim.y * gridDim.z;
;     unsigned sum, cnt, mine, sp = 0u;
;     for (;;) {
;         sum = 0u; cnt = 0u; mine = 0u;
; #pragma unroll
;         for (unsigned j = 0; j < 16; ++j) { const unsigned c = xb_ld(&bar[XB_XCNT(j)]); sum += c; cnt += (c > 0u) ? 1u : 0u; mine = (j == x) ? c : mine; }
;         if (sum == G) break;
;         __builtin_amdgcn_s_sleep(1);
;         if ((++sp & 255u) == 0u) { if (xb_ld(&bar[XB_TMO])) break; if (sp > XB_SPIN_CAP) { atomicAdd(&bar[XB_TMO], 1u); break; } }
;     }
;     nloc = mine > 0u ? mine : 1u; nx = cnt > 0u ? cnt : 1u;
; }
.Lxbar2_spin:
	global_load_dwordx4 v[4:7], v20, s[10:11] sc1
	global_load_dwordx4 v[8:11], v20, s[10:11] offset:16 sc1
	s_waitcnt vmcnt(0)
	v_add3_u32 v1, v4, v5, v6
	v_add3_u32 v1, v1, v7, v8
	v_add3_u32 v1, v1, v9, v10
	v_add_u32_e32 v1, v1, v11
	v_cmp_ge_u32_e32 vcc, v1, v3
	s_cbranch_vccnz .Lxbar2_done
	s_sleep 1
	s_add_i32 s6, s6, 1
	s_cmp_lt_u32 s6, 0x80000
	s_cbranch_scc1 .Lxbar2_spin
